# mixer queue: Q-blocks 15..8 run as whole items (were two half items each), 7..0 still split
# baseline (speedup 1.0000x reference)
.LBB0_476:
	v_readlane_b32 s0, v254, 24
	s_waitcnt lgkmcnt(0)
	s_barrier
	v_mov_b32_e32 v0, s0
	ds_read_b32 v0, v0
	s_waitcnt lgkmcnt(0)
	v_readfirstlane_b32 s48, v0
	s_cmp_eq_u32 s48, -1
	s_cbranch_scc1 .LBB0_509
	s_lshr_b32 s19, s48, 8
	s_and_b32 s57, s48, 0xff
	s_cmpk_lt_u32 s57, 0x58
	s_mov_b64 s[0:1], -1
	s_cbranch_scc0 .LBB0_846
	s_and_b32 s0, s48, 0xfc
	s_cmp_lg_u32 s0, 4
	s_mov_b64 s[0:1], -1
	s_cbranch_scc0 .LBB0_830
	s_cmp_gt_u32 s57, 3
	s_cbranch_scc0 .LBB0_797
	s_cmp_gt_u32 s57, 55
	s_cbranch_scc0 .LBB0_767
	s_cmp_gt_u32 s57, 71
	s_cbranch_scc1 .Lhalves_keep
	s_bitcmp1_b32 s57, 0
	s_cbranch_scc1 .LBB0_458
	s_sub_i32 s0, s57, 56
	s_lshr_b32 s0, s0, 1
	s_sub_i32 s30, 15, s0
	s_branch .Lwhole_entry
.Lhalves_keep:
	s_sub_i32 s0, s57, 56
	s_lshr_b32 s0, s0, 1
	s_sub_i32 s30, 15, s0
	s_and_b32 s18, s48, 1
	s_mov_b32 s44, s19
	v_mov_b32_e32 v0, v1
	s_ashr_i32 s45, s44, 31
	v_mbcnt_lo_u32_b32 v0, -1, v0
	v_mbcnt_hi_u32_b32 v42, -1, v0
	v_add_u32_e32 v2, s94, v42
	s_lshl_b64 s[0:1], s[44:45], 21
	v_readlane_b32 s12, v254, 34
	v_ashrrev_i32_e32 v4, 2, v2
	s_add_u32 s42, s12, s0
	v_readlane_b32 s0, v254, 35
	v_ashrrev_i32_e32 v5, 31, v4
	s_addc_u32 s43, s0, s1
	v_lshlrev_b64 v[4:5], 9, v[4:5]
	v_lshlrev_b32_e32 v0, 5, v42
	v_lshl_add_u64 v[4:5], s[42:43], 0, v[4:5]
	v_and_b32_e32 v0, 0x60, v0
	v_lshl_add_u64 v[8:9], v[4:5], 0, v[0:1]
	global_load_dwordx4 v[4:7], v[8:9], off offset:272
	s_nop 0
	global_load_dwordx4 v[8:11], v[8:9], off offset:256
	v_cmp_eq_u32_e64 s[26:27], 0, v42
	s_waitcnt vmcnt(0)
	v_and_b32_e32 v3, 0xffff0000, v8
	v_lshlrev_b32_e32 v0, 16, v8
	v_mul_f32_e32 v3, v3, v3
	v_and_b32_e32 v8, 0xffff0000, v9
	v_fmac_f32_e32 v3, v0, v0
	v_lshlrev_b32_e32 v0, 16, v9
	v_mul_f32_e32 v8, v8, v8
	v_fmac_f32_e32 v8, v0, v0
	v_add_f32_e32 v0, v3, v8
	v_and_b32_e32 v8, 0xffff0000, v10
	v_lshlrev_b32_e32 v3, 16, v10
	v_mul_f32_e32 v8, v8, v8
	v_fmac_f32_e32 v8, v3, v3
	v_add_f32_e32 v0, v8, v0
	v_and_b32_e32 v8, 0xffff0000, v11
	v_lshlrev_b32_e32 v3, 16, v11
	v_mul_f32_e32 v8, v8, v8
	v_fmac_f32_e32 v8, v3, v3
	v_lshlrev_b32_e32 v3, 16, v4
	v_and_b32_e32 v4, 0xffff0000, v4
	v_mul_f32_e32 v4, v4, v4
	v_add_f32_e32 v0, v8, v0
	v_fmac_f32_e32 v4, v3, v3
	v_add_f32_e32 v0, v4, v0
	v_and_b32_e32 v4, 0xffff0000, v5
	v_lshlrev_b32_e32 v3, 16, v5
	v_mul_f32_e32 v4, v4, v4
	v_fmac_f32_e32 v4, v3, v3
	v_add_f32_e32 v0, v4, v0
	v_and_b32_e32 v4, 0xffff0000, v6
	v_lshlrev_b32_e32 v3, 16, v6
	v_mul_f32_e32 v4, v4, v4
	v_fmac_f32_e32 v4, v3, v3
	v_add_f32_e32 v0, v4, v0
	v_and_b32_e32 v4, 0xffff0000, v7
	v_lshlrev_b32_e32 v3, 16, v7
	v_mul_f32_e32 v4, v4, v4
	v_fmac_f32_e32 v4, v3, v3
	v_add_f32_e32 v0, v4, v0
	s_nop 1
	v_add_f32_dpp v0, v0, v0 quad_perm:[1,0,3,2] row_mask:0xf bank_mask:0xf bound_ctrl:1
	s_nop 1
	v_add_f32_dpp v0, v0, v0 quad_perm:[2,3,0,1] row_mask:0xf bank_mask:0xf bound_ctrl:1
	s_nop 1
	v_add_f32_dpp v0, v0, v0 row_half_mirror row_mask:0xf bank_mask:0xf bound_ctrl:1
	s_nop 1
	v_add_f32_dpp v0, v0, v0 row_mirror row_mask:0xf bank_mask:0xf bound_ctrl:1
	v_mov_b32_e32 v3, v0
	s_nop 1
	v_permlane16_swap_b32_e32 v0, v3
	v_add_f32_e32 v0, v0, v3
	v_mov_b32_e32 v3, v0
	s_nop 1
	v_permlane32_swap_b32_e32 v0, v3
	s_and_saveexec_b64 s[0:1], s[26:27]
	s_cbranch_execz .LBB0_483
	v_readlane_b32 s12, v252, 18
	v_add_f32_e32 v0, v0, v3
	s_nop 0
	v_mov_b32_e32 v3, s12
	ds_write_b32 v3, v0

.Lwhole_entry:
	s_mov_b32 s18, 2
	s_mov_b32 s44, s19
	v_mov_b32_e32 v0, v1
	s_ashr_i32 s45, s44, 31
	v_mbcnt_lo_u32_b32 v0, -1, v0
	v_mbcnt_hi_u32_b32 v42, -1, v0
	v_add_u32_e32 v2, s94, v42
	s_lshl_b64 s[0:1], s[44:45], 21
	v_readlane_b32 s12, v254, 34
	v_ashrrev_i32_e32 v4, 2, v2
	s_add_u32 s42, s12, s0
	v_readlane_b32 s0, v254, 35
	v_ashrrev_i32_e32 v5, 31, v4
	s_addc_u32 s43, s0, s1
	v_lshlrev_b64 v[4:5], 9, v[4:5]
	v_lshlrev_b32_e32 v0, 5, v42
	v_lshl_add_u64 v[4:5], s[42:43], 0, v[4:5]
	v_and_b32_e32 v0, 0x60, v0
	v_lshl_add_u64 v[8:9], v[4:5], 0, v[0:1]
	global_load_dwordx4 v[4:7], v[8:9], off offset:272
	s_nop 0
	global_load_dwordx4 v[8:11], v[8:9], off offset:256
	v_cmp_eq_u32_e64 s[26:27], 0, v42
	s_waitcnt vmcnt(0)
	v_and_b32_e32 v3, 0xffff0000, v8
	v_lshlrev_b32_e32 v0, 16, v8
	v_mul_f32_e32 v3, v3, v3
	v_and_b32_e32 v8, 0xffff0000, v9
	v_fmac_f32_e32 v3, v0, v0
	v_lshlrev_b32_e32 v0, 16, v9
	v_mul_f32_e32 v8, v8, v8
	v_fmac_f32_e32 v8, v0, v0
	v_add_f32_e32 v0, v3, v8
	v_and_b32_e32 v8, 0xffff0000, v10
	v_lshlrev_b32_e32 v3, 16, v10
	v_mul_f32_e32 v8, v8, v8
	v_fmac_f32_e32 v8, v3, v3
	v_add_f32_e32 v0, v8, v0
	v_and_b32_e32 v8, 0xffff0000, v11
	v_lshlrev_b32_e32 v3, 16, v11
	v_mul_f32_e32 v8, v8, v8
	v_fmac_f32_e32 v8, v3, v3
	v_lshlrev_b32_e32 v3, 16, v4
	v_and_b32_e32 v4, 0xffff0000, v4
	v_mul_f32_e32 v4, v4, v4
	v_add_f32_e32 v0, v8, v0
	v_fmac_f32_e32 v4, v3, v3
	v_add_f32_e32 v0, v4, v0
	v_and_b32_e32 v4, 0xffff0000, v5
	v_lshlrev_b32_e32 v3, 16, v5
	v_mul_f32_e32 v4, v4, v4
	v_fmac_f32_e32 v4, v3, v3
	v_add_f32_e32 v0, v4, v0
	v_and_b32_e32 v4, 0xffff0000, v6
	v_lshlrev_b32_e32 v3, 16, v6
	v_mul_f32_e32 v4, v4, v4
	v_fmac_f32_e32 v4, v3, v3
	v_add_f32_e32 v0, v4, v0
	v_and_b32_e32 v4, 0xffff0000, v7
	v_lshlrev_b32_e32 v3, 16, v7
	v_mul_f32_e32 v4, v4, v4
	v_fmac_f32_e32 v4, v3, v3
	v_add_f32_e32 v0, v4, v0
	s_nop 1
	v_add_f32_dpp v0, v0, v0 quad_perm:[1,0,3,2] row_mask:0xf bank_mask:0xf bound_ctrl:1
	s_nop 1
	v_add_f32_dpp v0, v0, v0 quad_perm:[2,3,0,1] row_mask:0xf bank_mask:0xf bound_ctrl:1
	s_nop 1
	v_add_f32_dpp v0, v0, v0 row_half_mirror row_mask:0xf bank_mask:0xf bound_ctrl:1
	s_nop 1
	v_add_f32_dpp v0, v0, v0 row_mirror row_mask:0xf bank_mask:0xf bound_ctrl:1
	v_mov_b32_e32 v3, v0
	s_nop 1
	v_permlane16_swap_b32_e32 v0, v3
	v_add_f32_e32 v0, v0, v3
	v_mov_b32_e32 v3, v0
	s_nop 1
	v_permlane32_swap_b32_e32 v0, v3
	s_and_saveexec_b64 s[0:1], s[26:27]
	s_cbranch_execz .LBB0_770
	v_readlane_b32 s12, v252, 18
	v_add_f32_e32 v0, v0, v3
	s_nop 0
	v_mov_b32_e32 v3, s12
	ds_write_b32 v3, v0
